# ph3: router-weight prologue loads issued together (was 31 dependent round trips); next-batch row prefetch moved behind the trip's gamma/beta waits; router bias load hoisted out of the batch loop
# speedup vs baseline: 1.0230x; 1.0044x over previous
; __device__ __forceinline__ void unpack8(const u32x4 w, float (&f)[8]) { f[0] = bf_lo(w.x); f[1] = bf_hi(w.x); f[2] = bf_lo(w.y); f[3] = bf_hi(w.y); f[4] = bf_lo(w.z); f[5] = bf_hi(w.z); f[6] = bf_lo(w.w); f[7] = bf_hi(w.w); }
; __device__ __forceinline__ u32x4 pack8(const float (&f)[8]) { u32x4 o; o.x = cvt_pk_bf16(f[0], f[1]); o.y = cvt_pk_bf16(f[2], f[3]); o.z = cvt_pk_bf16(f[4], f[5]); o.w = cvt_pk_bf16(f[6], f[7]); return o; }
; __global__ void __launch_bounds__(NWAVES * 64, 2) mk_fwd(Args args) {
;     ...
;             if (tid < 32) LCNT[tid] = 0;
;             __syncthreads();
;             const int tk = lane & 15, kq = lane >> 4;
;             auto split8 = [](const float (&f)[8], bf16x8& hi, bf16x8& lo) { const u32x4 h = pack8(f); float fh[8], fl[8]; unpack8(h, fh);
; #pragma unroll
;                 for (int i = 0; i < 8; ++i) fl[i] = f[i] - fh[i];
;                 hi = __builtin_bit_cast(bf16x8, h); lo = __builtin_bit_cast(bf16x8, pack8(fl)); };
;             bf16x8 rwh[4][2], rwl[4][2];
; #pragma unroll
;             for (int ks = 0; ks < 4; ++ks)
; #pragma unroll
;                 for (int tile = 0; tile < 2; ++tile) { float f[8];
; #pragma unroll
;                     for (int j = 0; j < 8; ++j) f[j] = rw[(size_t)(128 * wave + 32 * ks + 8 * kq + j) * NEXP + 16 * tile + tk];
;                     split8(f, rwh[ks][tile], rwl[ks][tile]); }
;             int nbatch = 0;
;             for (int rep = 0; rep < NREP(3); ++rep) {
;             const bool dummy = rep + 1 < NREP(3);
;             bf16_t* XBo = dummy ? CAT : XB; unsigned char* XQo = dummy ? (unsigned char*)HB : ws + WS_XQ;
;             if (rep > 0) { __syncthreads(); if (tid < 32) LCNT[tid] = 0; __syncthreads(); }
;             nbatch = 0;
;             u32x4 yp[2][2];
;             {   const int b0 = bx < T / 16 ? bx : 0;
; #pragma unroll
;                 for (int ii = 0; ii < 2; ++ii) { const size_t t = (size_t)b0 * 16 + wave * 2 + ii; yp[ii][0] = *(const u32x4*)(YB + t * D + 8 * lane); yp[ii][1] = *(const u32x4*)(YB + t * D + 512 + 8 * lane); } }
.LBB0_481:
	s_mov_b32 s2, -1
	s_waitcnt lgkmcnt(0)
	s_barrier
	s_nop 0
	v_mbcnt_lo_u32_b32 v0, s2, 0
	v_mbcnt_hi_u32_b32 v106, s2, v0
	v_readlane_b32 s2, v253, 9
	s_nop 1
	v_add_u32_e32 v94, s2, v106
	v_cmp_gt_i32_e64 s[2:3], 32, v94
	v_lshl_add_u32 v107, v94, 2, 0
	s_and_saveexec_b64 s[4:5], s[2:3]
	v_add_u32_e32 v0, 0x14900, v107
	ds_write_b32 v0, v33
	s_or_b64 exec, exec, s[4:5]
	v_readlane_b32 s8, v252, 43
	s_lshl_b32 s4, s66, 11
	v_readlane_b32 s16, v252, 51
	v_readlane_b32 s17, v252, 52
	v_readlane_b32 s18, v252, 53
	v_readlane_b32 s19, v252, 54
	v_readlane_b32 s20, v252, 55
	v_readlane_b32 s21, v252, 56
	s_mov_b32 s5, s69
	s_mov_b32 s6, s4
	v_readlane_b32 s22, v252, 57
	v_readlane_b32 s23, v252, 58
	s_mov_b64 s[16:17], s[20:21]
	v_writelane_b32 v254, s6, 40
	s_lshl_b64 s[4:5], s[4:5], 2
	s_mov_b64 s[18:19], s[22:23]
	v_writelane_b32 v254, s7, 41
	v_readlane_b32 s9, v252, 44
	v_readlane_b32 s10, v252, 45
	v_readlane_b32 s11, v252, 46
	s_add_u32 s6, s18, s4
	s_addc_u32 s7, s19, s5
	v_readlane_b32 s8, v252, 0
	v_writelane_b32 v254, s6, 48
	v_readlane_b32 s9, v252, 1
	s_add_u32 s4, s8, s4
	v_writelane_b32 v254, s7, 49
	s_addc_u32 s5, s9, s5
	v_writelane_b32 v254, s4, 44
	s_mov_b32 s67, s69
	s_lshl_b64 s[40:41], s[66:67], 17
	v_writelane_b32 v254, s5, 45
	v_readlane_b32 s4, v253, 25
	v_readlane_b32 s5, v253, 26
	s_andn2_b64 vcc, exec, s[4:5]
	s_mov_b32 s6, 0
	v_readlane_b32 s12, v252, 47
	v_readlane_b32 s13, v252, 48
	v_readlane_b32 s14, v252, 49
	v_readlane_b32 s15, v252, 50
	v_readlane_b32 s10, v252, 2
	v_readlane_b32 s11, v252, 3
	s_waitcnt lgkmcnt(0)
	s_barrier
	s_cbranch_vccnz .LBB0_496
	s_lshl_b32 s68, s66, 5
	v_readlane_b32 s8, v252, 43
	s_lshl_b64 s[4:5], s[68:69], 2
	v_readlane_b32 s12, v252, 47
	v_readlane_b32 s13, v252, 48
	s_add_u32 s6, s12, s4
	v_lshlrev_b32_e32 v2, 3, v106
	s_addc_u32 s7, s13, s5
	v_ashrrev_i32_e32 v3, 31, v2
	v_readlane_b32 s4, v254, 48
	v_lshlrev_b64 v[0:1], 2, v[2:3]
	v_readlane_b32 s5, v254, 49
	v_readlane_b32 s9, v252, 44
	v_ashrrev_i32_e32 v5, 4, v106
	v_lshl_add_u64 v[96:97], s[4:5], 0, v[0:1]
	v_readlane_b32 s4, v254, 44
	v_readlane_b32 s5, v254, 45
	v_lshlrev_b32_e32 v6, 2, v94
	v_readlane_b32 s13, v255, 41
	v_lshl_add_u64 v[98:99], s[4:5], 0, v[0:1]
	v_and_b32_e32 v0, 31, v106
	v_lshlrev_b32_e32 v32, 2, v0
	v_readlane_b32 s8, v253, 28
	v_readlane_b32 s10, v252, 45
	v_and_b32_e32 v4, 15, v106
	v_ashrrev_i32_e32 v95, 5, v94
	v_and_b32_e32 v7, 0xffffff80, v6
	v_readlane_b32 s9, v255, 40
	v_add_u32_e32 v109, s13, v6
	s_add_i32 s4, 0, 0x14900
	v_mov_b32_e32 v6, s8
	s_movk_i32 s8, 0x1010
	v_lshl_add_u64 v[102:103], s[6:7], 0, v[32:33]
	s_add_i32 s6, 0, 0x1e800
	v_lshl_add_u32 v64, v5, 3, s42
	v_readlane_b32 s11, v252, 46
	v_add3_u32 v108, s9, v7, v32
	v_add_u32_e32 v110, s4, v32
	v_mad_u32_u24 v78, v4, s8, v6
	v_lshl_add_u32 v112, v95, 4, s6
	s_add_u32 s6, s10, s40
	s_addc_u32 s7, s11, s41
	v_lshlrev_b32_e32 v32, 2, v4
	v_lshlrev_b32_e32 v1, 5, v5
	v_lshlrev_b32_e32 v80, 2, v5
	v_lshl_add_u64 v[62:63], s[6:7], 0, v[32:33]
	v_add_u32_e32 v111, s13, v7
	v_readlane_b32 s6, v255, 15
	v_lshl_add_u64 v[100:101], s[36:37], 0, v[2:3]
	v_lshlrev_b64 v[2:3], 1, v[2:3]
	v_readlane_b32 s7, v255, 16
	v_readlane_b32 s14, v252, 49
	v_readlane_b32 s15, v252, 50
	v_add_u32_e32 v79, s9, v32
	s_mov_b32 s12, 0
	v_cmp_eq_u32_e64 s[4:5], 0, v106
	v_lshl_add_u32 v113, v106, 5, 0
	v_lshl_add_u64 v[104:105], s[94:95], 0, v[2:3]
	v_add_u32_e32 v114, v78, v1
	v_readlane_b32 s13, v255, 30
	v_readlane_b32 s14, v255, 19
	v_readlane_b32 s15, v252, 6
	v_readlane_b32 s16, v252, 51
	v_readlane_b32 s17, v252, 52
	v_readlane_b32 s18, v252, 53
	v_readlane_b32 s19, v252, 54
	v_readlane_b32 s20, v252, 55
	v_readlane_b32 s21, v252, 56
	v_readlane_b32 s22, v252, 57
	v_readlane_b32 s23, v252, 58
	v_lshl_add_u64 v[74:75], s[6:7], 0, v[2:3]
	v_readlane_b32 s6, v255, 28
	v_add_lshl_u32 v80, v80, s6, 7
	s_add_i32 s6, 0, 0x14a00
	v_lshl_add_u32 v32, v95, 6, s6
	v_add_u32_e32 v115, v79, v80
	v_ashrrev_i32_e32 v65, 31, v64
	v_lshlrev_b64 v[178:179], 7, v[64:65]
	s_mov_b64 s[98:99], 0x1000
	v_lshl_add_u64 v[178:179], v[62:63], 0, v[178:179]
	v_lshl_add_u64 v[180:181], v[178:179], 0, s[98:99]
	v_lshl_add_u64 v[182:183], v[180:181], 0, s[98:99]
	v_lshl_add_u64 v[184:185], v[182:183], 0, s[98:99]
	global_load_dword v4, v[184:185], off offset:64
	global_load_dword v8, v[184:185], off offset:192
	global_load_dword v5, v[184:185], off offset:320
	global_load_dword v9, v[184:185], off offset:448
	global_load_dword v6, v[184:185], off offset:576
	global_load_dword v10, v[184:185], off offset:704
	global_load_dword v7, v[184:185], off offset:832
	global_load_dword v11, v[184:185], off offset:960
	global_load_dword v12, v[184:185], off
	global_load_dword v16, v[184:185], off offset:128
	global_load_dword v13, v[184:185], off offset:256
	global_load_dword v17, v[184:185], off offset:384
	global_load_dword v14, v[184:185], off offset:512
	global_load_dword v18, v[184:185], off offset:640
	global_load_dword v15, v[184:185], off offset:768
	global_load_dword v19, v[184:185], off offset:896
	global_load_dword v20, v[182:183], off offset:64
	global_load_dword v24, v[182:183], off offset:192
	global_load_dword v21, v[182:183], off offset:320
	global_load_dword v25, v[182:183], off offset:448
	global_load_dword v22, v[182:183], off offset:576
	global_load_dword v26, v[182:183], off offset:704
	global_load_dword v23, v[182:183], off offset:832
	global_load_dword v27, v[182:183], off offset:960
	global_load_dword v28, v[182:183], off
	global_load_dword v34, v[182:183], off offset:128
	global_load_dword v29, v[182:183], off offset:256
	global_load_dword v35, v[182:183], off offset:384
; __global__ void __launch_bounds__(NWAVES * 64, 2) mk_fwd(Args args) {
;     ...
;             bf16x8 rwh[4][2], rwl[4][2];
; #pragma unroll
;             for (int ks = 0; ks < 4; ++ks)
; #pragma unroll
;                 for (int tile = 0; tile < 2; ++tile) { float f[8];
; #pragma unroll
;                     for (int j = 0; j < 8; ++j) f[j] = rw[(size_t)(128 * wave + 32 * ks + 8 * kq + j) * NEXP + 16 * tile + tk];
;                     split8(f, rwh[ks][tile], rwl[ks][tile]); }
;             int nbatch = 0;
;             for (int rep = 0; rep < NREP(3); ++rep) {
;             const bool dummy = rep + 1 < NREP(3);
;             bf16_t* XBo = dummy ? CAT : XB; unsigned char* XQo = dummy ? (unsigned char*)HB : ws + WS_XQ;
;             if (rep > 0) { __syncthreads(); if (tid < 32) LCNT[tid] = 0; __syncthreads(); }
;             nbatch = 0;
;             u32x4 yp[2][2];
;             {   const int b0 = bx < T / 16 ? bx : 0;
; #pragma unroll
;                 for (int ii = 0; ii < 2; ++ii) { const size_t t = (size_t)b0 * 16 + wave * 2 + ii; yp[ii][0] = *(const u32x4*)(YB + t * D + 8 * lane); yp[ii][1] = *(const u32x4*)(YB + t * D + 512 + 8 * lane); } }
	global_load_dword v30, v[182:183], off offset:512
	global_load_dword v36, v[182:183], off offset:640
	global_load_dword v31, v[182:183], off offset:768
	global_load_dword v37, v[182:183], off offset:896
	global_load_dword v38, v[180:181], off offset:64
	global_load_dword v42, v[180:181], off offset:192
	global_load_dword v39, v[180:181], off offset:320
	global_load_dword v43, v[180:181], off offset:448
	global_load_dword v40, v[180:181], off offset:576
	global_load_dword v44, v[180:181], off offset:704
	global_load_dword v41, v[180:181], off offset:832
	global_load_dword v45, v[180:181], off offset:960
	global_load_dword v46, v[180:181], off
	global_load_dword v50, v[180:181], off offset:128
	global_load_dword v47, v[180:181], off offset:256
	global_load_dword v51, v[180:181], off offset:384
	global_load_dword v48, v[180:181], off offset:512
	global_load_dword v52, v[180:181], off offset:640
	global_load_dword v49, v[180:181], off offset:768
	global_load_dword v53, v[180:181], off offset:896
	global_load_dword v54, v[178:179], off offset:64
	global_load_dword v58, v[178:179], off offset:192
	global_load_dword v55, v[178:179], off offset:320
	global_load_dword v59, v[178:179], off offset:448
	global_load_dword v56, v[178:179], off offset:576
	global_load_dword v60, v[178:179], off offset:704
	global_load_dword v57, v[178:179], off offset:832
	global_load_dword v61, v[178:179], off offset:960
	global_load_dword v62, v[178:179], off
	global_load_dword v66, v[178:179], off offset:128
	global_load_dword v63, v[178:179], off offset:256
	global_load_dword v67, v[178:179], off offset:384
	global_load_dword v64, v[178:179], off offset:512
	global_load_dword v68, v[178:179], off offset:640
	global_load_dword v65, v[178:179], off offset:768
	global_load_dword v69, v[178:179], off offset:896
	global_load_dwordx4 v[82:85], v[74:75], off offset:3072
	global_load_dwordx4 v[78:81], v[74:75], off offset:2048
	global_load_dwordx4 v[70:73], v[74:75], off offset:1024
	s_nop 0
	global_load_dwordx4 v[74:77], v[74:75], off
	global_load_dword v249, v[102:103], off
	s_waitcnt vmcnt(61)
	v_cvt_pk_bf16_f32 v186, v4, v8
	v_cvt_pk_bf16_f32 v187, v5, v9
	v_cvt_pk_bf16_f32 v188, v6, v10
	v_cvt_pk_bf16_f32 v189, v7, v11
	v_lshlrev_b32_e32 v190, 16, v186
	v_and_b32_e32 v194, 0xffff0000, v186
	v_lshlrev_b32_e32 v191, 16, v187
	v_and_b32_e32 v195, 0xffff0000, v187
	v_lshlrev_b32_e32 v192, 16, v188
	v_and_b32_e32 v196, 0xffff0000, v188
	v_lshlrev_b32_e32 v193, 16, v189
	v_and_b32_e32 v197, 0xffff0000, v189
	v_sub_f32_e32 v4, v4, v190
	v_sub_f32_e32 v8, v8, v194
	v_sub_f32_e32 v5, v5, v191
	v_sub_f32_e32 v9, v9, v195
	v_sub_f32_e32 v6, v6, v192
	v_sub_f32_e32 v10, v10, v196
	v_sub_f32_e32 v7, v7, v193
	v_sub_f32_e32 v11, v11, v197
	v_cvt_pk_bf16_f32 v8, v4, v8
	v_cvt_pk_bf16_f32 v9, v5, v9
	v_cvt_pk_bf16_f32 v10, v6, v10
	v_cvt_pk_bf16_f32 v11, v7, v11
	v_mov_b32_e32 v4, v186
	v_mov_b32_e32 v5, v187
	v_mov_b32_e32 v6, v188
	v_mov_b32_e32 v7, v189
	s_waitcnt vmcnt(53)
	v_cvt_pk_bf16_f32 v186, v12, v16
	v_cvt_pk_bf16_f32 v187, v13, v17
	v_cvt_pk_bf16_f32 v188, v14, v18
	v_cvt_pk_bf16_f32 v189, v15, v19
	v_lshlrev_b32_e32 v190, 16, v186
	v_and_b32_e32 v194, 0xffff0000, v186
	v_lshlrev_b32_e32 v191, 16, v187
	v_and_b32_e32 v195, 0xffff0000, v187
	v_lshlrev_b32_e32 v192, 16, v188
	v_and_b32_e32 v196, 0xffff0000, v188
	v_lshlrev_b32_e32 v193, 16, v189
	v_and_b32_e32 v197, 0xffff0000, v189
	v_sub_f32_e32 v12, v12, v190
	v_sub_f32_e32 v16, v16, v194
	v_sub_f32_e32 v13, v13, v191
	v_sub_f32_e32 v17, v17, v195
	v_sub_f32_e32 v14, v14, v192
	v_sub_f32_e32 v18, v18, v196
	v_sub_f32_e32 v15, v15, v193
	v_sub_f32_e32 v19, v19, v197
	v_cvt_pk_bf16_f32 v16, v12, v16
	v_cvt_pk_bf16_f32 v17, v13, v17
	v_cvt_pk_bf16_f32 v18, v14, v18
	v_cvt_pk_bf16_f32 v19, v15, v19
	v_mov_b32_e32 v12, v186
	v_mov_b32_e32 v13, v187
	v_mov_b32_e32 v14, v188
	v_mov_b32_e32 v15, v189
	s_waitcnt vmcnt(45)
	v_cvt_pk_bf16_f32 v186, v20, v24
	v_cvt_pk_bf16_f32 v187, v21, v25
	v_cvt_pk_bf16_f32 v188, v22, v26
	v_cvt_pk_bf16_f32 v189, v23, v27
	v_lshlrev_b32_e32 v190, 16, v186
	v_and_b32_e32 v194, 0xffff0000, v186
	v_lshlrev_b32_e32 v191, 16, v187
	v_and_b32_e32 v195, 0xffff0000, v187
	v_lshlrev_b32_e32 v192, 16, v188
	v_and_b32_e32 v196, 0xffff0000, v188
	v_lshlrev_b32_e32 v193, 16, v189
	v_and_b32_e32 v197, 0xffff0000, v189
	v_sub_f32_e32 v20, v20, v190
	v_sub_f32_e32 v24, v24, v194
	v_sub_f32_e32 v21, v21, v191
	v_sub_f32_e32 v25, v25, v195
	v_sub_f32_e32 v22, v22, v192
	v_sub_f32_e32 v26, v26, v196
	v_sub_f32_e32 v23, v23, v193
	v_sub_f32_e32 v27, v27, v197
	v_cvt_pk_bf16_f32 v24, v20, v24
	v_cvt_pk_bf16_f32 v25, v21, v25
	v_cvt_pk_bf16_f32 v26, v22, v26
	v_cvt_pk_bf16_f32 v27, v23, v27
	v_mov_b32_e32 v20, v186
	v_mov_b32_e32 v21, v187
	v_mov_b32_e32 v22, v188
	v_mov_b32_e32 v23, v189
	s_waitcnt vmcnt(37)
	v_cvt_pk_bf16_f32 v186, v28, v34
	v_cvt_pk_bf16_f32 v187, v29, v35
	v_cvt_pk_bf16_f32 v188, v30, v36
	v_cvt_pk_bf16_f32 v189, v31, v37
	v_lshlrev_b32_e32 v190, 16, v186
	v_and_b32_e32 v194, 0xffff0000, v186
	v_lshlrev_b32_e32 v191, 16, v187
	v_and_b32_e32 v195, 0xffff0000, v187
	v_lshlrev_b32_e32 v192, 16, v188
	v_and_b32_e32 v196, 0xffff0000, v188
	v_lshlrev_b32_e32 v193, 16, v189
	v_and_b32_e32 v197, 0xffff0000, v189
	v_sub_f32_e32 v28, v28, v190
	v_sub_f32_e32 v34, v34, v194
	v_sub_f32_e32 v29, v29, v191
	v_sub_f32_e32 v35, v35, v195
	v_sub_f32_e32 v30, v30, v192
	v_sub_f32_e32 v36, v36, v196
	v_sub_f32_e32 v31, v31, v193
	v_sub_f32_e32 v37, v37, v197
	v_cvt_pk_bf16_f32 v34, v28, v34
	v_cvt_pk_bf16_f32 v35, v29, v35
	v_cvt_pk_bf16_f32 v36, v30, v36
	v_cvt_pk_bf16_f32 v37, v31, v37
	v_mov_b32_e32 v28, v186
	v_mov_b32_e32 v29, v187
	v_mov_b32_e32 v30, v188
	v_mov_b32_e32 v31, v189
	s_waitcnt vmcnt(29)
; __device__ __forceinline__ void unpack8(const u32x4 w, float (&f)[8]) { f[0] = bf_lo(w.x); f[1] = bf_hi(w.x); f[2] = bf_lo(w.y); f[3] = bf_hi(w.y); f[4] = bf_lo(w.z); f[5] = bf_hi(w.z); f[6] = bf_lo(w.w); f[7] = bf_hi(w.w); }
; __global__ void __launch_bounds__(NWAVES * 64, 2) mk_fwd(Args args) {
;     ...
;             bf16x8 rwh[4][2], rwl[4][2];
; #pragma unroll
;             for (int ks = 0; ks < 4; ++ks)
; #pragma unroll
;                 for (int tile = 0; tile < 2; ++tile) { float f[8];
; #pragma unroll
;                     for (int j = 0; j < 8; ++j) f[j] = rw[(size_t)(128 * wave + 32 * ks + 8 * kq + j) * NEXP + 16 * tile + tk];
;                     split8(f, rwh[ks][tile], rwl[ks][tile]); }
;     ...
;             for (int bi = bx; bi < T / 16; bi += G, ++nbatch) {
;                 u32x4 yc[2][2];
; #pragma unroll
;                 for (int ii = 0; ii < 2; ++ii) { yc[ii][0] = yp[ii][0]; yc[ii][1] = yp[ii][1]; }
;                 {   const int bn = (bi + G < T / 16) ? bi + G : bi;
; #pragma unroll
;                     for (int ii = 0; ii < 2; ++ii) { const size_t t = (size_t)bn * 16 + wave * 2 + ii; yp[ii][0] = *(const u32x4*)(YB + t * D + 8 * lane); yp[ii][1] = *(const u32x4*)(YB + t * D + 512 + 8 * lane); } }
; #pragma unroll
;                 for (int ii = 0; ii < 2; ++ii) {
;                     const int tl = wave * 2 + ii, t = bi * 16 + tl;
;                     float v[16], o[16];
; #pragma unroll
;                     for (int hf = 0; hf < 2; ++hf) { float f[8]; unpack8(yc[ii][hf], f);
; #pragma unroll
;                         for (int i = 0; i < 8; ++i) v[8 * hf + i] = f[i]; }
;                     ln_row16(v, lng, lnb, lane, o);
	v_cvt_pk_bf16_f32 v186, v38, v42
	v_cvt_pk_bf16_f32 v187, v39, v43
	v_cvt_pk_bf16_f32 v188, v40, v44
	v_cvt_pk_bf16_f32 v189, v41, v45
	v_lshlrev_b32_e32 v190, 16, v186
	v_and_b32_e32 v194, 0xffff0000, v186
	v_lshlrev_b32_e32 v191, 16, v187
	v_and_b32_e32 v195, 0xffff0000, v187
	v_lshlrev_b32_e32 v192, 16, v188
	v_and_b32_e32 v196, 0xffff0000, v188
	v_lshlrev_b32_e32 v193, 16, v189
	v_and_b32_e32 v197, 0xffff0000, v189
	v_sub_f32_e32 v38, v38, v190
	v_sub_f32_e32 v42, v42, v194
	v_sub_f32_e32 v39, v39, v191
	v_sub_f32_e32 v43, v43, v195
	v_sub_f32_e32 v40, v40, v192
	v_sub_f32_e32 v44, v44, v196
	v_sub_f32_e32 v41, v41, v193
	v_sub_f32_e32 v45, v45, v197
	v_cvt_pk_bf16_f32 v42, v38, v42
	v_cvt_pk_bf16_f32 v43, v39, v43
	v_cvt_pk_bf16_f32 v44, v40, v44
	v_cvt_pk_bf16_f32 v45, v41, v45
	v_mov_b32_e32 v38, v186
	v_mov_b32_e32 v39, v187
	v_mov_b32_e32 v40, v188
	v_mov_b32_e32 v41, v189
	s_waitcnt vmcnt(21)
	v_cvt_pk_bf16_f32 v186, v46, v50
	v_cvt_pk_bf16_f32 v187, v47, v51
	v_cvt_pk_bf16_f32 v188, v48, v52
	v_cvt_pk_bf16_f32 v189, v49, v53
	v_lshlrev_b32_e32 v190, 16, v186
	v_and_b32_e32 v194, 0xffff0000, v186
	v_lshlrev_b32_e32 v191, 16, v187
	v_and_b32_e32 v195, 0xffff0000, v187
	v_lshlrev_b32_e32 v192, 16, v188
	v_and_b32_e32 v196, 0xffff0000, v188
	v_lshlrev_b32_e32 v193, 16, v189
	v_and_b32_e32 v197, 0xffff0000, v189
	v_sub_f32_e32 v46, v46, v190
	v_sub_f32_e32 v50, v50, v194
	v_sub_f32_e32 v47, v47, v191
	v_sub_f32_e32 v51, v51, v195
	v_sub_f32_e32 v48, v48, v192
	v_sub_f32_e32 v52, v52, v196
	v_sub_f32_e32 v49, v49, v193
	v_sub_f32_e32 v53, v53, v197
	v_cvt_pk_bf16_f32 v50, v46, v50
	v_cvt_pk_bf16_f32 v51, v47, v51
	v_cvt_pk_bf16_f32 v52, v48, v52
	v_cvt_pk_bf16_f32 v53, v49, v53
	v_mov_b32_e32 v46, v186
	v_mov_b32_e32 v47, v187
	v_mov_b32_e32 v48, v188
	v_mov_b32_e32 v49, v189
	s_waitcnt vmcnt(13)
	v_cvt_pk_bf16_f32 v186, v54, v58
	v_cvt_pk_bf16_f32 v187, v55, v59
	v_cvt_pk_bf16_f32 v188, v56, v60
	v_cvt_pk_bf16_f32 v189, v57, v61
	v_lshlrev_b32_e32 v190, 16, v186
	v_and_b32_e32 v194, 0xffff0000, v186
	v_lshlrev_b32_e32 v191, 16, v187
	v_and_b32_e32 v195, 0xffff0000, v187
	v_lshlrev_b32_e32 v192, 16, v188
	v_and_b32_e32 v196, 0xffff0000, v188
	v_lshlrev_b32_e32 v193, 16, v189
	v_and_b32_e32 v197, 0xffff0000, v189
	v_sub_f32_e32 v54, v54, v190
	v_sub_f32_e32 v58, v58, v194
	v_sub_f32_e32 v55, v55, v191
	v_sub_f32_e32 v59, v59, v195
	v_sub_f32_e32 v56, v56, v192
	v_sub_f32_e32 v60, v60, v196
	v_sub_f32_e32 v57, v57, v193
	v_sub_f32_e32 v61, v61, v197
	v_cvt_pk_bf16_f32 v58, v54, v58
	v_cvt_pk_bf16_f32 v59, v55, v59
	v_cvt_pk_bf16_f32 v60, v56, v60
	v_cvt_pk_bf16_f32 v61, v57, v61
	v_mov_b32_e32 v54, v186
	v_mov_b32_e32 v55, v187
	v_mov_b32_e32 v56, v188
	v_mov_b32_e32 v57, v189
	s_waitcnt vmcnt(5)
	v_cvt_pk_bf16_f32 v186, v62, v66
	v_cvt_pk_bf16_f32 v187, v63, v67
	v_cvt_pk_bf16_f32 v188, v64, v68
	v_cvt_pk_bf16_f32 v189, v65, v69
	v_lshlrev_b32_e32 v190, 16, v186
	v_and_b32_e32 v194, 0xffff0000, v186
	v_lshlrev_b32_e32 v191, 16, v187
	v_and_b32_e32 v195, 0xffff0000, v187
	v_lshlrev_b32_e32 v192, 16, v188
	v_and_b32_e32 v196, 0xffff0000, v188
	v_lshlrev_b32_e32 v193, 16, v189
	v_and_b32_e32 v197, 0xffff0000, v189
	v_sub_f32_e32 v62, v62, v190
	v_sub_f32_e32 v66, v66, v194
	v_sub_f32_e32 v63, v63, v191
	v_sub_f32_e32 v67, v67, v195
	v_sub_f32_e32 v64, v64, v192
	v_sub_f32_e32 v68, v68, v196
	v_sub_f32_e32 v65, v65, v193
	v_sub_f32_e32 v69, v69, v197
	v_cvt_pk_bf16_f32 v66, v62, v66
	v_cvt_pk_bf16_f32 v67, v63, v67
	v_cvt_pk_bf16_f32 v68, v64, v68
	v_cvt_pk_bf16_f32 v69, v65, v69
	v_mov_b32_e32 v62, v186
	v_mov_b32_e32 v63, v187
	v_mov_b32_e32 v64, v188
	v_mov_b32_e32 v65, v189
.LBB0_485:
	s_mov_b32 s6, s15
	s_add_i32 s15, s15, s72
	s_cmpk_gt_i32 s15, 0x7ff
	s_cselect_b64 s[8:9], -1, 0
	s_cmpk_lt_i32 s15, 0x800
	s_cselect_b32 s6, s15, s6
	s_ashr_i32 s7, s6, 31
	s_lshl_b64 s[6:7], s[6:7], 4
	v_readlane_b32 s10, v255, 19
	s_add_u32 s6, s6, s10
	s_addc_u32 s7, s7, 0
	s_lshl_b64 s[6:7], s[6:7], 11
	s_mov_b64 s[98:99], s[6:7]
	s_waitcnt vmcnt(0)
	v_mov_b64_e32 v[88:89], v[84:85]
	v_mov_b64_e32 v[92:93], v[80:81]
	v_mov_b64_e32 v[86:87], v[82:83]
	v_mov_b64_e32 v[90:91], v[78:79]
	v_mov_b64_e32 v[118:119], v[76:77]
	v_mov_b64_e32 v[122:123], v[72:73]
	v_mov_b64_e32 v[116:117], v[74:75]
	v_mov_b64_e32 v[120:121], v[70:71]
	global_load_dwordx4 v[124:127], v[96:97], off offset:16
	global_load_dwordx4 v[128:131], v[96:97], off
	global_load_dwordx4 v[132:135], v[98:99], off offset:16
	global_load_dwordx4 v[136:139], v[98:99], off
	v_lshlrev_b32_e32 v2, 16, v116
	v_and_b32_e32 v3, 0xffff0000, v116
	v_lshlrev_b32_e32 v152, 16, v117
	v_and_b32_e32 v153, 0xffff0000, v117
	v_lshlrev_b32_e32 v154, 16, v118
	v_and_b32_e32 v155, 0xffff0000, v118
	v_lshlrev_b32_e32 v156, 16, v119
	v_and_b32_e32 v157, 0xffff0000, v119
	global_load_dwordx4 v[116:119], v[96:97], off offset:2064
	global_load_dwordx4 v[140:143], v[96:97], off offset:2048
	global_load_dwordx4 v[144:147], v[98:99], off offset:2064
	global_load_dwordx4 v[148:151], v[98:99], off offset:2048
	v_lshlrev_b32_e32 v160, 16, v122
	v_and_b32_e32 v161, 0xffff0000, v122
	v_lshlrev_b32_e32 v122, 16, v123
	v_and_b32_e32 v123, 0xffff0000, v123
	v_lshlrev_b32_e32 v158, 16, v120
	v_and_b32_e32 v159, 0xffff0000, v120
	v_lshlrev_b32_e32 v120, 16, v121
	v_and_b32_e32 v121, 0xffff0000, v121
	v_add_f32_e32 v1, v123, v122
	v_add_f32_e32 v162, v161, v160
	v_add_f32_e32 v1, v162, v1
	v_add_f32_e32 v162, v121, v120
	v_add_f32_e32 v163, v159, v158
	v_add_f32_e32 v162, v163, v162
	v_add_f32_e32 v1, v162, v1
	v_add_f32_e32 v162, v157, v156
	v_add_f32_e32 v163, v155, v154
	v_add_f32_e32 v162, v163, v162
	v_add_f32_e32 v163, v153, v152
	v_add_f32_e32 v164, v3, v2
	v_add_f32_e32 v163, v164, v163
	v_add_f32_e32 v162, v163, v162
	v_add_f32_e32 v1, v162, v1
	s_mov_b32 s6, 0xf800000
	s_nop 0
	v_add_f32_dpp v1, v1, v1 quad_perm:[1,0,3,2] row_mask:0xf bank_mask:0xf bound_ctrl:1
	s_nop 1
	v_add_f32_dpp v1, v1, v1 quad_perm:[2,3,0,1] row_mask:0xf bank_mask:0xf bound_ctrl:1
	s_nop 1
	v_add_f32_dpp v1, v1, v1 row_half_mirror row_mask:0xf bank_mask:0xf bound_ctrl:1
	s_nop 1
	v_add_f32_dpp v1, v1, v1 row_mirror row_mask:0xf bank_mask:0xf bound_ctrl:1
	ds_swizzle_b32 v162, v1 offset:swizzle(SWAP,16)
	s_waitcnt lgkmcnt(0)
; __device__ __forceinline__ float wave_sum(float v) { v += dpp_f<0xB1>(v); v += dpp_f<0x4E>(v); v += dpp_f<0x141>(v); v += dpp_f<0x140>(v); v += xor_sw<16>(v); return sum_x32(v); }
; __device__ __forceinline__ float wave_max(float v) { v = fmaxf(v, dpp_f<0xB1>(v)); v = fmaxf(v, dpp_f<0x4E>(v)); v = fmaxf(v, dpp_f<0x141>(v)); v = fmaxf(v, dpp_f<0x140>(v)); v = fmaxf(v, xor_sw<16>(v)); return max_x32(v); }
; __device__ __forceinline__ void ln_row16(float (&v)[16], const float* lng, const float* lnb, int lane, float (&o)[16]) {
;     const float s = ((v[0] + v[1]) + (v[2] + v[3])) + ((v[4] + v[5]) + (v[6] + v[7])) + (((v[8] + v[9]) + (v[10] + v[11])) + ((v[12] + v[13]) + (v[14] + v[15])));
;     const float mean = wave_sum(s) * (1.0f / D);
; #pragma unroll
;     for (int i = 0; i < 16; ++i) v[i] -= mean;
;     const float s2 = ((v[0] * v[0] + v[1] * v[1]) + (v[2] * v[2] + v[3] * v[3])) + ((v[4] * v[4] + v[5] * v[5]) + (v[6] * v[6] + v[7] * v[7]))
;                    + (((v[8] * v[8] + v[9] * v[9]) + (v[10] * v[10] + v[11] * v[11])) + ((v[12] * v[12] + v[13] * v[13]) + (v[14] * v[14] + v[15] * v[15])));
;     const float rstd = 1.0f / sqrtf(wave_sum(s2) * (1.0f / D) + LN_EPS);
; #pragma unroll
;     for (int hf = 0; hf < 2; ++hf) { const int col = 512 * hf + 8 * lane;
;         const f32x4 g0 = *(const f32x4*)(lng + col), g1 = *(const f32x4*)(lng + col + 4), b0 = *(const f32x4*)(lnb + col), b1 = *(const f32x4*)(lnb + col + 4);
; #pragma unroll
;         for (int i = 0; i < 4; ++i) { o[8 * hf + i] = v[8 * hf + i] * rstd * g0[i] + b0[i]; o[8 * hf + 4 + i] = v[8 * hf + 4 + i] * rstd * g1[i] + b1[i]; } }
; }
; __device__ __forceinline__ float q8_row16(const float (&o)[16], unsigned char* qrow, int lane) {
;     float am = 0.f;
; #pragma unroll
;     for (int i = 0; i < 16; ++i) am = fmaxf(am, fabsf(o[i]));
;     am = wave_max(am);
	v_add_f32_e32 v1, v1, v162
	v_mov_b32_e32 v162, v1
	s_nop 1
	v_permlane32_swap_b32_e32 v1, v162
	v_add_f32_e32 v1, v1, v162
	v_mul_f32_e32 v162, 0x3a800000, v1
	v_pk_add_f32 v[2:3], v[2:3], v[162:163] op_sel_hi:[1,0] neg_lo:[0,1] neg_hi:[0,1]
	v_pk_add_f32 v[152:153], v[152:153], v[162:163] op_sel_hi:[1,0] neg_lo:[0,1] neg_hi:[0,1]
	v_pk_add_f32 v[154:155], v[154:155], v[162:163] op_sel_hi:[1,0] neg_lo:[0,1] neg_hi:[0,1]
	v_pk_add_f32 v[156:157], v[156:157], v[162:163] op_sel_hi:[1,0] neg_lo:[0,1] neg_hi:[0,1]
	v_pk_add_f32 v[158:159], v[158:159], v[162:163] op_sel_hi:[1,0] neg_lo:[0,1] neg_hi:[0,1]
	v_pk_add_f32 v[164:165], v[120:121], v[162:163] op_sel_hi:[1,0] neg_lo:[0,1] neg_hi:[0,1]
	v_pk_add_f32 v[160:161], v[160:161], v[162:163] op_sel_hi:[1,0] neg_lo:[0,1] neg_hi:[0,1]
	v_pk_add_f32 v[162:163], v[122:123], v[162:163] op_sel_hi:[1,0] neg_lo:[0,1] neg_hi:[0,1]
	v_pk_mul_f32 v[120:121], v[2:3], v[2:3]
	v_pk_mul_f32 v[122:123], v[152:153], v[152:153]
	v_pk_mul_f32 v[166:167], v[154:155], v[154:155]
	v_pk_mul_f32 v[168:169], v[156:157], v[156:157]
	v_pk_mul_f32 v[170:171], v[158:159], v[158:159]
	v_pk_mul_f32 v[172:173], v[164:165], v[164:165]
	v_pk_mul_f32 v[174:175], v[160:161], v[160:161]
	v_pk_mul_f32 v[176:177], v[162:163], v[162:163]
	v_add_f32_e32 v174, v174, v175
	v_add_f32_e32 v1, v176, v177
	v_add_f32_e32 v172, v172, v173
	v_add_f32_e32 v170, v170, v171
	v_add_f32_e32 v168, v168, v169
	v_add_f32_e32 v166, v166, v167
	v_add_f32_e32 v122, v122, v123
	v_add_f32_e32 v120, v120, v121
	v_add_f32_e32 v1, v174, v1
	v_add_f32_e32 v170, v170, v172
	v_add_f32_e32 v166, v166, v168
	v_add_f32_e32 v120, v120, v122
	v_add_f32_e32 v1, v170, v1
	v_add_f32_e32 v120, v120, v166
	v_add_f32_e32 v1, v120, v1
	s_nop 1
	v_add_f32_dpp v1, v1, v1 quad_perm:[1,0,3,2] row_mask:0xf bank_mask:0xf bound_ctrl:1
	s_nop 1
	v_add_f32_dpp v1, v1, v1 quad_perm:[2,3,0,1] row_mask:0xf bank_mask:0xf bound_ctrl:1
	s_nop 1
	v_add_f32_dpp v1, v1, v1 row_half_mirror row_mask:0xf bank_mask:0xf bound_ctrl:1
	s_nop 1
	v_add_f32_dpp v1, v1, v1 row_mirror row_mask:0xf bank_mask:0xf bound_ctrl:1
	ds_swizzle_b32 v120, v1 offset:swizzle(SWAP,16)
	s_waitcnt lgkmcnt(0)
	v_add_f32_e32 v1, v1, v120
	v_mov_b32_e32 v120, v1
	s_nop 1
	v_permlane32_swap_b32_e32 v1, v120
	v_add_f32_e32 v1, v1, v120
	v_fmamk_f32 v1, v1, 0x3a800000, v250
	v_cmp_gt_f32_e32 vcc, s6, v1
	v_mul_f32_e32 v120, 0x4f800000, v1
	s_nop 0
	v_cndmask_b32_e32 v1, v1, v120, vcc
	v_sqrt_f32_e32 v120, v1
	s_nop 0
	v_add_u32_e32 v121, -1, v120
	v_fma_f32 v122, -v121, v120, v1
	v_cmp_ge_f32_e64 s[6:7], 0, v122
	v_add_u32_e32 v122, 1, v120
	s_nop 0
	v_cndmask_b32_e64 v121, v120, v121, s[6:7]
	v_fma_f32 v120, -v122, v120, v1
	v_cmp_lt_f32_e64 s[6:7], 0, v120
	s_nop 1
	v_cndmask_b32_e64 v120, v121, v122, s[6:7]
	v_mul_f32_e32 v121, 0x37800000, v120
	v_cndmask_b32_e32 v120, v120, v121, vcc
	v_cmp_class_f32_e32 vcc, v1, v251
	s_nop 1
	v_cndmask_b32_e32 v1, v120, v1, vcc
	v_div_scale_f32 v120, s[6:7], v1, v1, 1.0
	v_rcp_f32_e32 v121, v120
	s_mul_i32 s6, s73, 0x2020
	v_fma_f32 v122, -v120, v121, 1.0
	v_fmac_f32_e32 v121, v122, v121
	v_div_scale_f32 v122, vcc, 1.0, v1, 1.0
	v_mul_f32_e32 v123, v122, v121
	v_fma_f32 v166, -v120, v123, v122
	v_fmac_f32_e32 v123, v166, v121
	v_fma_f32 v120, -v120, v123, v122
	v_div_fmas_f32 v120, v120, v121, v123
	v_div_fixup_f32 v166, v120, v1, 1.0
	v_pk_mul_f32 v[2:3], v[2:3], v[166:167] op_sel_hi:[1,0]
	v_add_u32_e32 v1, s6, v113
	s_waitcnt vmcnt(4)
	v_pk_fma_f32 v[120:121], v[128:129], v[2:3], v[136:137]
	v_pk_mul_f32 v[2:3], v[154:155], v[166:167] op_sel_hi:[1,0]
	v_readlane_b32 s6, v255, 36
	v_pk_fma_f32 v[124:125], v[124:125], v[2:3], v[132:133]
	v_pk_mul_f32 v[2:3], v[152:153], v[166:167] op_sel_hi:[1,0]
	s_add_i32 s10, s6, s14
	v_pk_fma_f32 v[122:123], v[130:131], v[2:3], v[138:139]
	v_pk_mul_f32 v[2:3], v[156:157], v[166:167] op_sel_hi:[1,0]
	s_ashr_i32 s11, s10, 31
	v_pk_fma_f32 v[126:127], v[126:127], v[2:3], v[134:135]
	v_pk_mul_f32 v[2:3], v[158:159], v[166:167] op_sel_hi:[1,0]
	s_lshl_b64 s[6:7], s[10:11], 10
	s_waitcnt vmcnt(0)
	v_pk_fma_f32 v[128:129], v[140:141], v[2:3], v[148:149]
	v_pk_mul_f32 v[2:3], v[160:161], v[166:167] op_sel_hi:[1,0]
	s_nop 0
	v_pk_fma_f32 v[116:117], v[116:117], v[2:3], v[144:145]
	v_pk_mul_f32 v[2:3], v[164:165], v[166:167] op_sel_hi:[1,0]
	s_nop 0
	v_pk_fma_f32 v[130:131], v[142:143], v[2:3], v[150:151]
	v_pk_mul_f32 v[2:3], v[162:163], v[166:167] op_sel_hi:[1,0]
	s_nop 0
	v_pk_fma_f32 v[118:119], v[118:119], v[2:3], v[146:147]
	ds_write_b128 v1, v[120:123]
	ds_write_b128 v1, v[124:127] offset:16
	ds_write_b128 v1, v[128:131] offset:2048
	ds_write_b128 v1, v[116:119] offset:2064
	v_max3_f32 v1, |v120|, 0, |v121|
	v_max3_f32 v1, v1, |v122|, |v123|
	v_max3_f32 v1, v1, |v124|, |v125|
	v_max3_f32 v1, v1, |v126|, |v127|
	v_max3_f32 v1, v1, |v128|, |v129|
	v_max3_f32 v1, v1, |v130|, |v131|
	v_max3_f32 v1, v1, |v116|, |v117|
	v_max3_f32 v1, v1, |v118|, |v119|
	s_nop 1
	v_mov_b32_dpp v2, v1 quad_perm:[1,0,3,2] row_mask:0xf bank_mask:0xf bound_ctrl:1
	v_max_f32_e32 v2, v2, v2
	v_max_f32_e32 v1, v1, v2
	s_nop 1
	v_mov_b32_dpp v2, v1 quad_perm:[2,3,0,1] row_mask:0xf bank_mask:0xf bound_ctrl:1
	v_max_f32_e32 v2, v2, v2
	v_max_f32_e32 v1, v1, v2
	s_nop 1
	v_mov_b32_dpp v2, v1 row_half_mirror row_mask:0xf bank_mask:0xf bound_ctrl:1
	v_max_f32_e32 v2, v2, v2
	v_max_f32_e32 v1, v1, v2
	s_nop 1
	v_mov_b32_dpp v2, v1 row_mirror row_mask:0xf bank_mask:0xf bound_ctrl:1
	v_max_f32_e32 v2, v2, v2
	v_max_f32_e32 v1, v1, v2
	ds_swizzle_b32 v2, v1 offset:swizzle(SWAP,16)
	s_waitcnt lgkmcnt(0)
; __device__ __forceinline__ float wave_sum(float v) { v += dpp_f<0xB1>(v); v += dpp_f<0x4E>(v); v += dpp_f<0x141>(v); v += dpp_f<0x140>(v); v += xor_sw<16>(v); return sum_x32(v); }
; __device__ __forceinline__ float wave_max(float v) { v = fmaxf(v, dpp_f<0xB1>(v)); v = fmaxf(v, dpp_f<0x4E>(v)); v = fmaxf(v, dpp_f<0x141>(v)); v = fmaxf(v, dpp_f<0x140>(v)); v = fmaxf(v, xor_sw<16>(v)); return max_x32(v); }
; __device__ __forceinline__ void ln_row16(float (&v)[16], const float* lng, const float* lnb, int lane, float (&o)[16]) {
;     const float s = ((v[0] + v[1]) + (v[2] + v[3])) + ((v[4] + v[5]) + (v[6] + v[7])) + (((v[8] + v[9]) + (v[10] + v[11])) + ((v[12] + v[13]) + (v[14] + v[15])));
;     const float mean = wave_sum(s) * (1.0f / D);
; #pragma unroll
;     for (int i = 0; i < 16; ++i) v[i] -= mean;
;     const float s2 = ((v[0] * v[0] + v[1] * v[1]) + (v[2] * v[2] + v[3] * v[3])) + ((v[4] * v[4] + v[5] * v[5]) + (v[6] * v[6] + v[7] * v[7]))
;                    + (((v[8] * v[8] + v[9] * v[9]) + (v[10] * v[10] + v[11] * v[11])) + ((v[12] * v[12] + v[13] * v[13]) + (v[14] * v[14] + v[15] * v[15])));
; __device__ __forceinline__ float q8_row16(const float (&o)[16], unsigned char* qrow, int lane) {
;     float am = 0.f;
; #pragma unroll
;     for (int i = 0; i < 16; ++i) am = fmaxf(am, fabsf(o[i]));
;     am = wave_max(am);
;     const float qs = am > 0.f ? am * (1.0f / 127.0f) : 1.0f, qinv = 1.0f / qs;
; #pragma unroll
;     for (int hf = 0; hf < 2; ++hf) { u32x2 q; q.x = q8x4(o[8 * hf], o[8 * hf + 1], o[8 * hf + 2], o[8 * hf + 3], qinv); q.y = q8x4(o[8 * hf + 4], o[8 * hf + 5], o[8 * hf + 6], o[8 * hf + 7], qinv);
;         *(u32x2*)(qrow + 512 * hf + 8 * lane) = q; }
;     return qs;
; }
	v_max_f32_e32 v2, v2, v2
	v_max_f32_e32 v1, v1, v2
	v_mov_b32_e32 v2, v1
	s_nop 1
	v_permlane32_swap_b32_e32 v1, v2
	v_max_f32_e32 v2, v2, v2
	v_max_f32_e32 v1, v1, v1
	v_max_f32_e32 v1, v1, v2
	v_cmp_lt_f32_e32 vcc, 0, v1
	v_mul_f32_e32 v1, 0x3c010204, v1
	s_nop 0
	v_cndmask_b32_e32 v1, 1.0, v1, vcc
	v_div_scale_f32 v2, s[16:17], v1, v1, 1.0
	v_rcp_f32_e32 v3, v2
	s_nop 0
	v_fma_f32 v132, -v2, v3, 1.0
	v_fmac_f32_e32 v3, v132, v3
	v_div_scale_f32 v132, vcc, 1.0, v1, 1.0
	v_mul_f32_e32 v133, v132, v3
	v_fma_f32 v134, -v2, v133, v132
	v_fmac_f32_e32 v133, v134, v3
	v_fma_f32 v2, -v2, v133, v132
	v_div_fmas_f32 v2, v2, v3, v133
	v_div_fixup_f32 v132, v2, v1, 1.0
	v_fmaak_f32 v120, v120, v132, 0x4b400000
	v_fmaak_f32 v121, v121, v132, 0x4b400000
	v_fmaak_f32 v122, v122, v132, 0x4b400000
	v_fmaak_f32 v123, v123, v132, 0x4b400000
	v_perm_b32 v122, v123, v122, s61
	v_perm_b32 v120, v121, v120, s61
	v_perm_b32 v120, v122, v120, s79
	v_fmaak_f32 v121, v124, v132, 0x4b400000
	v_fmaak_f32 v122, v125, v132, 0x4b400000
	v_fmaak_f32 v123, v126, v132, 0x4b400000
	v_fmaak_f32 v124, v127, v132, 0x4b400000
	v_perm_b32 v123, v124, v123, s61
	v_perm_b32 v121, v122, v121, s61
	v_lshl_add_u64 v[2:3], v[100:101], 0, s[6:7]
	v_perm_b32 v121, v123, v121, s79
	global_store_dwordx2 v[2:3], v[120:121], off
	v_fmaak_f32 v120, v128, v132, 0x4b400000
	v_fmaak_f32 v121, v129, v132, 0x4b400000
	v_fmaak_f32 v122, v130, v132, 0x4b400000
	v_fmaak_f32 v123, v131, v132, 0x4b400000
	v_fmaak_f32 v116, v116, v132, 0x4b400000
	v_fmaak_f32 v117, v117, v132, 0x4b400000
	v_fmaak_f32 v118, v118, v132, 0x4b400000
	v_fmaak_f32 v119, v119, v132, 0x4b400000
	v_perm_b32 v122, v123, v122, s61
	v_perm_b32 v120, v121, v120, s61
	v_perm_b32 v118, v119, v118, s61
	v_perm_b32 v116, v117, v116, s61
	v_perm_b32 v120, v122, v120, s79
	v_perm_b32 v121, v118, v116, s79
	global_store_dwordx2 v[2:3], v[120:121], off offset:512
	s_and_saveexec_b64 s[6:7], s[4:5]
	s_add_i32 s11, s13, -4
	v_mov_b32_e32 v2, s11
	ds_write_b32 v2, v1
	s_or_b64 exec, exec, s[6:7]
	v_lshlrev_b32_e32 v150, 16, v88
	v_and_b32_e32 v151, 0xffff0000, v88
	v_lshlrev_b32_e32 v152, 16, v89
	v_and_b32_e32 v153, 0xffff0000, v89
	v_lshlrev_b32_e32 v146, 16, v86
	v_and_b32_e32 v147, 0xffff0000, v86
	v_lshlrev_b32_e32 v148, 16, v87
	v_and_b32_e32 v149, 0xffff0000, v87
	v_add_f32_e32 v1, v153, v152
	v_add_f32_e32 v86, v151, v150
	v_add_f32_e32 v1, v86, v1
	v_add_f32_e32 v86, v149, v148
	v_add_f32_e32 v87, v147, v146
	v_lshlrev_b32_e32 v142, 16, v92
	v_and_b32_e32 v143, 0xffff0000, v92
	v_lshlrev_b32_e32 v144, 16, v93
	v_and_b32_e32 v145, 0xffff0000, v93
	v_add_f32_e32 v86, v87, v86
	global_load_dwordx4 v[116:119], v[96:97], off offset:16
	global_load_dwordx4 v[120:123], v[96:97], off
	global_load_dwordx4 v[124:127], v[98:99], off offset:16
	global_load_dwordx4 v[128:131], v[98:99], off
	v_lshlrev_b32_e32 v2, 16, v90
	v_and_b32_e32 v3, 0xffff0000, v90
	v_lshlrev_b32_e32 v140, 16, v91
	v_and_b32_e32 v141, 0xffff0000, v91
	v_add_f32_e32 v1, v86, v1
	v_add_f32_e32 v86, v145, v144
	v_add_f32_e32 v87, v143, v142
	v_add_f32_e32 v86, v87, v86
	v_add_f32_e32 v87, v141, v140
	v_add_f32_e32 v88, v3, v2
	v_add_f32_e32 v87, v88, v87
	v_add_f32_e32 v86, v87, v86
	v_add_f32_e32 v1, v86, v1
	global_load_dwordx4 v[86:89], v[96:97], off offset:2064
	global_load_dwordx4 v[90:93], v[96:97], off offset:2048
	global_load_dwordx4 v[132:135], v[98:99], off offset:2064
	global_load_dwordx4 v[136:139], v[98:99], off offset:2048
	v_add_f32_dpp v1, v1, v1 quad_perm:[1,0,3,2] row_mask:0xf bank_mask:0xf bound_ctrl:1
	s_mov_b32 s6, 0xf800000
	s_nop 0
	v_add_f32_dpp v1, v1, v1 quad_perm:[2,3,0,1] row_mask:0xf bank_mask:0xf bound_ctrl:1
	s_nop 1
	v_add_f32_dpp v1, v1, v1 row_half_mirror row_mask:0xf bank_mask:0xf bound_ctrl:1
	s_nop 1
	v_add_f32_dpp v1, v1, v1 row_mirror row_mask:0xf bank_mask:0xf bound_ctrl:1
	ds_swizzle_b32 v154, v1 offset:swizzle(SWAP,16)
	s_waitcnt lgkmcnt(0)
	v_add_f32_e32 v1, v1, v154
	v_mov_b32_e32 v154, v1
	s_nop 1
	v_permlane32_swap_b32_e32 v1, v154
	v_add_f32_e32 v1, v1, v154
	v_mul_f32_e32 v154, 0x3a800000, v1
	v_pk_add_f32 v[2:3], v[2:3], v[154:155] op_sel_hi:[1,0] neg_lo:[0,1] neg_hi:[0,1]
	v_pk_add_f32 v[140:141], v[140:141], v[154:155] op_sel_hi:[1,0] neg_lo:[0,1] neg_hi:[0,1]
	v_pk_add_f32 v[142:143], v[142:143], v[154:155] op_sel_hi:[1,0] neg_lo:[0,1] neg_hi:[0,1]
	v_pk_add_f32 v[144:145], v[144:145], v[154:155] op_sel_hi:[1,0] neg_lo:[0,1] neg_hi:[0,1]
	v_pk_add_f32 v[146:147], v[146:147], v[154:155] op_sel_hi:[1,0] neg_lo:[0,1] neg_hi:[0,1]
	v_pk_add_f32 v[148:149], v[148:149], v[154:155] op_sel_hi:[1,0] neg_lo:[0,1] neg_hi:[0,1]
	v_pk_add_f32 v[150:151], v[150:151], v[154:155] op_sel_hi:[1,0] neg_lo:[0,1] neg_hi:[0,1]
	v_pk_add_f32 v[152:153], v[152:153], v[154:155] op_sel_hi:[1,0] neg_lo:[0,1] neg_hi:[0,1]
	v_pk_mul_f32 v[154:155], v[2:3], v[2:3]
	v_pk_mul_f32 v[156:157], v[140:141], v[140:141]
	v_pk_mul_f32 v[158:159], v[142:143], v[142:143]
	v_pk_mul_f32 v[160:161], v[144:145], v[144:145]
	v_pk_mul_f32 v[162:163], v[146:147], v[146:147]
	v_pk_mul_f32 v[164:165], v[148:149], v[148:149]
	v_pk_mul_f32 v[166:167], v[150:151], v[150:151]
	v_pk_mul_f32 v[168:169], v[152:153], v[152:153]
	v_add_f32_e32 v166, v166, v167
	v_add_f32_e32 v1, v168, v169
	v_add_f32_e32 v164, v164, v165
	v_add_f32_e32 v162, v162, v163
	v_add_f32_e32 v160, v160, v161
	v_add_f32_e32 v158, v158, v159
	v_add_f32_e32 v156, v156, v157
	v_add_f32_e32 v154, v154, v155
	v_add_f32_e32 v1, v166, v1
	v_add_f32_e32 v162, v162, v164
	v_add_f32_e32 v158, v158, v160
	v_add_f32_e32 v154, v154, v156
	v_add_f32_e32 v1, v162, v1
	v_add_f32_e32 v154, v154, v158
	v_add_f32_e32 v1, v154, v1
	s_nop 1
	v_add_f32_dpp v1, v1, v1 quad_perm:[1,0,3,2] row_mask:0xf bank_mask:0xf bound_ctrl:1
	s_nop 1
	v_add_f32_dpp v1, v1, v1 quad_perm:[2,3,0,1] row_mask:0xf bank_mask:0xf bound_ctrl:1
	s_nop 1
	v_add_f32_dpp v1, v1, v1 row_half_mirror row_mask:0xf bank_mask:0xf bound_ctrl:1
	s_nop 1
	v_add_f32_dpp v1, v1, v1 row_mirror row_mask:0xf bank_mask:0xf bound_ctrl:1
	ds_swizzle_b32 v154, v1 offset:swizzle(SWAP,16)
	s_waitcnt lgkmcnt(0)
; #define LAS __attribute__((address_space(3)))
; __device__ __forceinline__ void unpack8(const u32x4 w, float (&f)[8]) { f[0] = bf_lo(w.x); f[1] = bf_hi(w.x); f[2] = bf_lo(w.y); f[3] = bf_hi(w.y); f[4] = bf_lo(w.z); f[5] = bf_hi(w.z); f[6] = bf_lo(w.w); f[7] = bf_hi(w.w); }
; __global__ void __launch_bounds__(NWAVES * 64, 2) mk_fwd(Args args) {
;     ...
;             for (int bi = bx; bi < T / 16; bi += G, ++nbatch) {
;                 u32x4 yc[2][2];
; #pragma unroll
;                 for (int ii = 0; ii < 2; ++ii) { yc[ii][0] = yp[ii][0]; yc[ii][1] = yp[ii][1]; }
;                 {   const int bn = (bi + G < T / 16) ? bi + G : bi;
; #pragma unroll
;                     for (int ii = 0; ii < 2; ++ii) { const size_t t = (size_t)bn * 16 + wave * 2 + ii; yp[ii][0] = *(const u32x4*)(YB + t * D + 8 * lane); yp[ii][1] = *(const u32x4*)(YB + t * D + 512 + 8 * lane); } }
; #pragma unroll
;                 for (int ii = 0; ii < 2; ++ii) {
;                     const int tl = wave * 2 + ii, t = bi * 16 + tl;
;                     float v[16], o[16];
; #pragma unroll
;                     for (int hf = 0; hf < 2; ++hf) { float f[8]; unpack8(yc[ii][hf], f);
; #pragma unroll
;                         for (int i = 0; i < 8; ++i) v[8 * hf + i] = f[i]; }
;                     ln_row16(v, lng, lnb, lane, o);
; #pragma unroll
;                     for (int hf = 0; hf < 2; ++hf) { const int col = 512 * hf + 8 * lane;
;                         *(LAS f32x4*)(XL + tl * XS + col) = (f32x4){o[8 * hf], o[8 * hf + 1], o[8 * hf + 2], o[8 * hf + 3]}; *(LAS f32x4*)(XL + tl * XS + col + 4) = (f32x4){o[8 * hf + 4], o[8 * hf + 5], o[8 * hf + 6], o[8 * hf + 7]}; }
;                     const float qs = q8_row16(o, XQo + (size_t)t * D, lane);
;                     if (lane == 0) TSC[nbatch * 16 + tl] = qs;
;                 }
;                 __syncthreads();
	v_add_f32_e32 v1, v1, v154
	v_mov_b32_e32 v154, v1
	s_nop 1
	v_permlane32_swap_b32_e32 v1, v154
	v_add_f32_e32 v1, v1, v154
	v_fmamk_f32 v1, v1, 0x3a800000, v250
	v_mul_f32_e32 v154, 0x4f800000, v1
	v_cmp_gt_f32_e32 vcc, s6, v1
	s_nop 1
	v_cndmask_b32_e32 v1, v1, v154, vcc
	v_sqrt_f32_e32 v154, v1
	s_nop 0
	v_add_u32_e32 v155, -1, v154
	v_fma_f32 v156, -v155, v154, v1
	v_cmp_ge_f32_e64 s[6:7], 0, v156
	v_add_u32_e32 v156, 1, v154
	s_nop 0
	v_cndmask_b32_e64 v155, v154, v155, s[6:7]
	v_fma_f32 v154, -v156, v154, v1
	v_cmp_lt_f32_e64 s[6:7], 0, v154
	s_nop 1
	v_cndmask_b32_e64 v154, v155, v156, s[6:7]
	v_mul_f32_e32 v155, 0x37800000, v154
	v_cndmask_b32_e32 v154, v154, v155, vcc
	v_cmp_class_f32_e32 vcc, v1, v251
	s_nop 1
	v_cndmask_b32_e32 v1, v154, v1, vcc
	v_div_scale_f32 v154, s[6:7], v1, v1, 1.0
	v_rcp_f32_e32 v155, v154
	v_readlane_b32 s6, v255, 21
	v_fma_f32 v156, -v154, v155, 1.0
	v_fmac_f32_e32 v155, v156, v155
	v_div_scale_f32 v156, vcc, 1.0, v1, 1.0
	v_mul_f32_e32 v157, v156, v155
	v_fma_f32 v158, -v154, v157, v156
	v_fmac_f32_e32 v157, v158, v155
	v_fma_f32 v154, -v154, v157, v156
	v_div_fmas_f32 v154, v154, v155, v157
	v_div_fixup_f32 v154, v154, v1, 1.0
	v_pk_mul_f32 v[2:3], v[2:3], v[154:155] op_sel_hi:[1,0]
	v_add_u32_e32 v1, s6, v113
	s_waitcnt vmcnt(4)
	v_pk_fma_f32 v[120:121], v[120:121], v[2:3], v[128:129]
	v_pk_mul_f32 v[2:3], v[142:143], v[154:155] op_sel_hi:[1,0]
	s_nop 0
	v_pk_fma_f32 v[116:117], v[116:117], v[2:3], v[124:125]
	v_pk_mul_f32 v[2:3], v[140:141], v[154:155] op_sel_hi:[1,0]
	s_nop 0
	v_pk_fma_f32 v[122:123], v[122:123], v[2:3], v[130:131]
	v_pk_mul_f32 v[2:3], v[144:145], v[154:155] op_sel_hi:[1,0]
	s_nop 0
	v_pk_fma_f32 v[118:119], v[118:119], v[2:3], v[126:127]
	v_pk_mul_f32 v[2:3], v[146:147], v[154:155] op_sel_hi:[1,0]
	s_waitcnt vmcnt(0)
	s_and_b64 vcc, exec, s[8:9]
	s_cbranch_vccnz .Lph3_no_prefetch
	v_lshl_add_u64 v[246:247], v[104:105], 0, s[98:99]
	global_load_dwordx4 v[74:77], v[246:247], off
	global_load_dwordx4 v[70:73], v[246:247], off offset:1024
	global_load_dwordx4 v[78:81], v[246:247], off offset:2048
	global_load_dwordx4 v[82:85], v[246:247], off offset:3072
.Lph3_no_prefetch:
	v_pk_fma_f32 v[90:91], v[90:91], v[2:3], v[136:137]
	v_pk_mul_f32 v[2:3], v[150:151], v[154:155] op_sel_hi:[1,0]
	s_nop 0
	v_pk_fma_f32 v[86:87], v[86:87], v[2:3], v[132:133]
	v_pk_mul_f32 v[2:3], v[148:149], v[154:155] op_sel_hi:[1,0]
	s_nop 0
	v_pk_fma_f32 v[92:93], v[92:93], v[2:3], v[138:139]
	v_pk_mul_f32 v[2:3], v[152:153], v[154:155] op_sel_hi:[1,0]
	s_nop 0
	v_pk_fma_f32 v[88:89], v[88:89], v[2:3], v[134:135]
	v_max3_f32 v2, |v120|, 0, |v121|
	v_max3_f32 v2, v2, |v122|, |v123|
	v_max3_f32 v2, v2, |v116|, |v117|
	v_max3_f32 v2, v2, |v118|, |v119|
	v_max3_f32 v2, v2, |v90|, |v91|
	v_max3_f32 v2, v2, |v92|, |v93|
	v_max3_f32 v2, v2, |v86|, |v87|
	v_max3_f32 v2, v2, |v88|, |v89|
	ds_write_b128 v1, v[120:123]
	ds_write_b128 v1, v[116:119] offset:16
	ds_write_b128 v1, v[90:93] offset:2048
	ds_write_b128 v1, v[86:89] offset:2064
	v_mov_b32_dpp v3, v2 quad_perm:[1,0,3,2] row_mask:0xf bank_mask:0xf bound_ctrl:1
	v_max_f32_e32 v3, v3, v3
	v_max_f32_e32 v2, v2, v3
	s_nop 1
	v_mov_b32_dpp v3, v2 quad_perm:[2,3,0,1] row_mask:0xf bank_mask:0xf bound_ctrl:1
	v_max_f32_e32 v3, v3, v3
	v_max_f32_e32 v2, v2, v3
	s_nop 1
	v_mov_b32_dpp v3, v2 row_half_mirror row_mask:0xf bank_mask:0xf bound_ctrl:1
	v_max_f32_e32 v3, v3, v3
	v_max_f32_e32 v2, v2, v3
	s_nop 1
	v_mov_b32_dpp v3, v2 row_mirror row_mask:0xf bank_mask:0xf bound_ctrl:1
	v_max_f32_e32 v3, v3, v3
	v_max_f32_e32 v2, v2, v3
	ds_swizzle_b32 v3, v2 offset:swizzle(SWAP,16)
	s_waitcnt lgkmcnt(0)
	v_max_f32_e32 v1, v3, v3
	v_max_f32_e32 v1, v2, v1
	v_mov_b32_e32 v2, v1
	s_nop 1
	v_permlane32_swap_b32_e32 v1, v2
	v_max_f32_e32 v2, v2, v2
	v_max_f32_e32 v1, v1, v1
	v_max_f32_e32 v1, v1, v2
	v_mul_f32_e32 v2, 0x3c010204, v1
	v_cmp_lt_f32_e32 vcc, 0, v1
	s_nop 1
	v_cndmask_b32_e32 v1, 1.0, v2, vcc
	v_div_scale_f32 v2, s[6:7], v1, v1, 1.0
	v_rcp_f32_e32 v3, v2
	s_add_i32 s6, s10, 1
	s_ashr_i32 s7, s6, 31
	s_lshl_b64 s[6:7], s[6:7], 10
	v_fma_f32 v124, -v2, v3, 1.0
	v_fmac_f32_e32 v3, v124, v3
	v_div_scale_f32 v124, vcc, 1.0, v1, 1.0
	v_mul_f32_e32 v125, v124, v3
	v_fma_f32 v126, -v2, v125, v124
	v_fmac_f32_e32 v125, v126, v3
	v_fma_f32 v2, -v2, v125, v124
	v_div_fmas_f32 v2, v2, v3, v125
	v_div_fixup_f32 v124, v2, v1, 1.0
	v_fmaak_f32 v120, v120, v124, 0x4b400000
	v_fmaak_f32 v121, v121, v124, 0x4b400000
	v_fmaak_f32 v122, v122, v124, 0x4b400000
	v_fmaak_f32 v123, v123, v124, 0x4b400000
	v_fmaak_f32 v116, v116, v124, 0x4b400000
	v_fmaak_f32 v117, v117, v124, 0x4b400000
	v_fmaak_f32 v118, v118, v124, 0x4b400000
	v_fmaak_f32 v119, v119, v124, 0x4b400000
	v_fmaak_f32 v90, v90, v124, 0x4b400000
	v_fmaak_f32 v91, v91, v124, 0x4b400000
	v_fmaak_f32 v92, v92, v124, 0x4b400000
	v_fmaak_f32 v93, v93, v124, 0x4b400000
	v_fmaak_f32 v86, v86, v124, 0x4b400000
	v_fmaak_f32 v87, v87, v124, 0x4b400000
	v_fmaak_f32 v88, v88, v124, 0x4b400000
	v_fmaak_f32 v89, v89, v124, 0x4b400000
	v_perm_b32 v122, v123, v122, s61
	v_perm_b32 v120, v121, v120, s61
	v_perm_b32 v118, v119, v118, s61
	v_perm_b32 v116, v117, v116, s61
	v_perm_b32 v92, v93, v92, s61
	v_perm_b32 v90, v91, v90, s61
	v_perm_b32 v88, v89, v88, s61
	v_perm_b32 v86, v87, v86, s61
	v_lshl_add_u64 v[2:3], v[100:101], 0, s[6:7]
	v_perm_b32 v120, v122, v120, s79
	v_perm_b32 v121, v118, v116, s79
	v_perm_b32 v90, v92, v90, s79
	v_perm_b32 v91, v88, v86, s79
	global_store_dwordx2 v[2:3], v[120:121], off
	global_store_dwordx2 v[2:3], v[90:91], off offset:512
	s_and_saveexec_b64 s[6:7], s[4:5]
	v_mov_b32_e32 v2, s13
	ds_write_b32 v2, v1
	s_or_b64 exec, exec, s[6:7]
	s_waitcnt lgkmcnt(0)
	s_barrier
; #define LAS __attribute__((address_space(3)))
; __global__ void __launch_bounds__(NWAVES * 64, 2) mk_fwd(Args args) {
;     ...
;                 {
;                     f32x4 a0 = (f32x4){0.f, 0.f, 0.f, 0.f}, a1 = (f32x4){0.f, 0.f, 0.f, 0.f};
; #pragma unroll
;                     for (int ks = 0; ks < 4; ++ks) { const LAS float* xp = XL + tk * XS + 128 * wave + 32 * ks + 8 * kq; const f32x4 p = *(const LAS f32x4*)xp, q = *(const LAS f32x4*)(xp + 4);
;                         const float f[8] = {p[0], p[1], p[2], p[3], q[0], q[1], q[2], q[3]}; bf16x8 xh, xl; split8(f, xh, xl);
;                         a0 = __builtin_amdgcn_mfma_f32_16x16x32_bf16(xh, rwh[ks][0], a0, 0, 0, 0); a1 = __builtin_amdgcn_mfma_f32_16x16x32_bf16(xh, rwh[ks][1], a1, 0, 0, 0);
;                         a0 = __builtin_amdgcn_mfma_f32_16x16x32_bf16(xh, rwl[ks][0], a0, 0, 0, 0); a1 = __builtin_amdgcn_mfma_f32_16x16x32_bf16(xh, rwl[ks][1], a1, 0, 0, 0);
;                         a0 = __builtin_amdgcn_mfma_f32_16x16x32_bf16(xl, rwh[ks][0], a0, 0, 0, 0); a1 = __builtin_amdgcn_mfma_f32_16x16x32_bf16(xl, rwh[ks][1], a1, 0, 0, 0); }
; #pragma unroll
;                     for (int r = 0; r < 4; ++r) { PART[(wave * 16 + 4 * kq + r) * 32 + tk] = a0[r]; PART[(wave * 16 + 4 * kq + r) * 32 + 16 + tk] = a1[r]; }
;                 }
;                 __syncthreads();
	ds_read_b128 v[86:89], v114
	ds_read_b128 v[90:93], v114 offset:16
	s_waitcnt lgkmcnt(1)
	v_cvt_pk_bf16_f32 v116, v86, v87
	v_cvt_pk_bf16_f32 v117, v88, v89
	s_waitcnt lgkmcnt(0)
	v_cvt_pk_bf16_f32 v118, v90, v91
	v_cvt_pk_bf16_f32 v119, v92, v93
	v_lshlrev_b32_e32 v2, 16, v116
	v_and_b32_e32 v3, 0xffff0000, v116
	v_pk_add_f32 v[2:3], v[86:87], v[2:3] neg_lo:[0,1] neg_hi:[0,1]
	v_lshlrev_b32_e32 v86, 16, v117
	v_and_b32_e32 v87, 0xffff0000, v117
	v_lshlrev_b32_e32 v120, 16, v118
	v_and_b32_e32 v121, 0xffff0000, v118
	v_pk_add_f32 v[124:125], v[88:89], v[86:87] neg_lo:[0,1] neg_hi:[0,1]
	v_mfma_f32_16x16x32_bf16 v[86:89], v[116:119], v[62:65], 0
	v_add_f32_e64 v126, v90, -v120
	v_add_f32_e64 v127, v91, -v121
	v_lshlrev_b32_e32 v90, 16, v119
	v_and_b32_e32 v91, 0xffff0000, v119
	v_mfma_f32_16x16x32_bf16 v[120:123], v[116:119], v[54:57], 0
	v_add_f32_e64 v128, v92, -v90
	v_add_f32_e64 v129, v93, -v91
	v_cvt_pk_bf16_f32 v90, v2, v3
	v_cvt_pk_bf16_f32 v91, v124, v125
	v_mfma_f32_16x16x32_bf16 v[86:89], v[116:119], v[66:69], v[86:89]
	v_cvt_pk_bf16_f32 v92, v126, v127
	v_cvt_pk_bf16_f32 v93, v128, v129
	v_mfma_f32_16x16x32_bf16 v[116:119], v[116:119], v[58:61], v[120:123]
	s_nop 2
	ds_read_b128 v[120:123], v114 offset:128
	ds_read_b128 v[124:127], v114 offset:144
	v_mfma_f32_16x16x32_bf16 v[86:89], v[90:93], v[62:65], v[86:89]
	v_mfma_f32_16x16x32_bf16 v[90:93], v[90:93], v[54:57], v[116:119]
	s_waitcnt lgkmcnt(1)
	s_nop 1
	v_cvt_pk_bf16_f32 v116, v120, v121
	v_cvt_pk_bf16_f32 v117, v122, v123
	s_waitcnt lgkmcnt(0)
	v_cvt_pk_bf16_f32 v118, v124, v125
	v_cvt_pk_bf16_f32 v119, v126, v127
	v_lshlrev_b32_e32 v2, 16, v116
	v_and_b32_e32 v3, 0xffff0000, v116
	v_pk_add_f32 v[2:3], v[120:121], v[2:3] neg_lo:[0,1] neg_hi:[0,1]
	v_lshlrev_b32_e32 v120, 16, v117
	v_and_b32_e32 v121, 0xffff0000, v117
	v_mfma_f32_16x16x32_bf16 v[86:89], v[116:119], v[46:49], v[86:89]
	v_add_f32_e64 v122, v122, -v120
	v_add_f32_e64 v123, v123, -v121
	v_lshlrev_b32_e32 v120, 16, v118
	v_and_b32_e32 v121, 0xffff0000, v118
	v_mfma_f32_16x16x32_bf16 v[90:93], v[116:119], v[38:41], v[90:93]
	v_add_f32_e64 v124, v124, -v120
	v_add_f32_e64 v125, v125, -v121
	v_lshlrev_b32_e32 v120, 16, v119
	v_and_b32_e32 v121, 0xffff0000, v119
	v_pk_add_f32 v[126:127], v[126:127], v[120:121] neg_lo:[0,1] neg_hi:[0,1]
	v_mfma_f32_16x16x32_bf16 v[86:89], v[116:119], v[50:53], v[86:89]
	v_cvt_pk_bf16_f32 v120, v2, v3
	v_cvt_pk_bf16_f32 v121, v122, v123
	v_cvt_pk_bf16_f32 v122, v124, v125
	v_mfma_f32_16x16x32_bf16 v[90:93], v[116:119], v[42:45], v[90:93]
	v_cvt_pk_bf16_f32 v123, v126, v127
	ds_read_b128 v[116:119], v114 offset:256
	ds_read_b128 v[124:127], v114 offset:272
	v_mfma_f32_16x16x32_bf16 v[86:89], v[120:123], v[46:49], v[86:89]
	v_mfma_f32_16x16x32_bf16 v[90:93], v[120:123], v[38:41], v[90:93]
	s_waitcnt lgkmcnt(1)
	v_cvt_pk_bf16_f32 v120, v116, v117
	v_cvt_pk_bf16_f32 v121, v118, v119
	s_waitcnt lgkmcnt(0)
	v_cvt_pk_bf16_f32 v122, v124, v125
	v_cvt_pk_bf16_f32 v123, v126, v127
	v_lshlrev_b32_e32 v2, 16, v120
	v_and_b32_e32 v3, 0xffff0000, v120
	v_pk_add_f32 v[2:3], v[116:117], v[2:3] neg_lo:[0,1] neg_hi:[0,1]
	v_lshlrev_b32_e32 v116, 16, v121
	v_and_b32_e32 v117, 0xffff0000, v121
	v_mfma_f32_16x16x32_bf16 v[86:89], v[120:123], v[28:31], v[86:89]
	v_add_f32_e64 v118, v118, -v116
	v_add_f32_e64 v119, v119, -v117
	v_lshlrev_b32_e32 v116, 16, v122
	v_and_b32_e32 v117, 0xffff0000, v122
	v_mfma_f32_16x16x32_bf16 v[90:93], v[120:123], v[20:23], v[90:93]
	v_add_f32_e64 v124, v124, -v116
	v_add_f32_e64 v125, v125, -v117
	v_lshlrev_b32_e32 v116, 16, v123
	v_and_b32_e32 v117, 0xffff0000, v123
	v_pk_add_f32 v[126:127], v[126:127], v[116:117] neg_lo:[0,1] neg_hi:[0,1]
	v_mfma_f32_16x16x32_bf16 v[86:89], v[120:123], v[34:37], v[86:89]
	v_cvt_pk_bf16_f32 v116, v2, v3
	v_cvt_pk_bf16_f32 v117, v118, v119
	v_cvt_pk_bf16_f32 v118, v124, v125
	v_mfma_f32_16x16x32_bf16 v[90:93], v[120:123], v[24:27], v[90:93]
	v_cvt_pk_bf16_f32 v119, v126, v127
	ds_read_b128 v[120:123], v114 offset:384
	ds_read_b128 v[124:127], v114 offset:400
	v_mfma_f32_16x16x32_bf16 v[86:89], v[116:119], v[28:31], v[86:89]
	v_mfma_f32_16x16x32_bf16 v[90:93], v[116:119], v[20:23], v[90:93]
	s_waitcnt lgkmcnt(1)
	v_cvt_pk_bf16_f32 v116, v120, v121
	v_cvt_pk_bf16_f32 v117, v122, v123
	s_waitcnt lgkmcnt(0)
	v_cvt_pk_bf16_f32 v118, v124, v125
	v_cvt_pk_bf16_f32 v119, v126, v127
	v_lshlrev_b32_e32 v2, 16, v116
	v_and_b32_e32 v3, 0xffff0000, v116
	v_pk_add_f32 v[2:3], v[120:121], v[2:3] neg_lo:[0,1] neg_hi:[0,1]
	v_lshlrev_b32_e32 v120, 16, v117
	v_and_b32_e32 v121, 0xffff0000, v117
	v_pk_add_f32 v[122:123], v[122:123], v[120:121] neg_lo:[0,1] neg_hi:[0,1]
	v_mfma_f32_16x16x32_bf16 v[86:89], v[116:119], v[12:15], v[86:89]
	v_lshlrev_b32_e32 v120, 16, v118
	v_and_b32_e32 v121, 0xffff0000, v118
	v_pk_add_f32 v[124:125], v[124:125], v[120:121] neg_lo:[0,1] neg_hi:[0,1]
	v_mfma_f32_16x16x32_bf16 v[90:93], v[116:119], v[4:7], v[90:93]
	v_lshlrev_b32_e32 v120, 16, v119
	v_and_b32_e32 v121, 0xffff0000, v119
	v_pk_add_f32 v[126:127], v[126:127], v[120:121] neg_lo:[0,1] neg_hi:[0,1]
	v_cvt_pk_bf16_f32 v120, v2, v3
	v_cvt_pk_bf16_f32 v121, v122, v123
	v_cvt_pk_bf16_f32 v122, v124, v125
	v_cvt_pk_bf16_f32 v123, v126, v127
	v_mfma_f32_16x16x32_bf16 v[86:89], v[116:119], v[16:19], v[86:89]
	v_mfma_f32_16x16x32_bf16 v[90:93], v[116:119], v[8:11], v[90:93]
	v_mfma_f32_16x16x32_bf16 v[86:89], v[120:123], v[12:15], v[86:89]
	v_mfma_f32_16x16x32_bf16 v[90:93], v[120:123], v[4:7], v[90:93]
	s_nop 7
	ds_write2_b32 v115, v86, v90 offset1:16
	ds_write2_b32 v115, v87, v91 offset0:32 offset1:48
	ds_write2_b32 v115, v88, v92 offset0:64 offset1:80
	ds_write2_b32 v115, v89, v93 offset0:96 offset1:112
	s_waitcnt lgkmcnt(0)
	s_barrier
; #define LAS __attribute__((address_space(3)))
; __global__ void __launch_bounds__(NWAVES * 64, 2) mk_fwd(Args args) {
;     ...
;                 {   const int tq = tid >> 5, e = tid & 31; float s = rb[e];
; #pragma unroll
;                     for (int w = 0; w < 8; ++w) s += PART[(w * 16 + tq) * 32 + e];
;                     const unsigned ub = __float_as_uint(s), key = (((ub >> 31) ? ~ub : (ub | 0x80000000u)) & ~31u) | (unsigned)(31 - e);
;                     ((LAS unsigned*)LOG)[tq * 32 + e] = key;
;                     asm volatile("s_waitcnt lgkmcnt(0)" ::: "memory");
;                     int rank = 0;
; #pragma unroll
;                     for (int q = 0; q < 8; ++q) { const u32x4 t4 = *(const LAS u32x4*)((LAS unsigned*)LOG + tq * 32 + 4 * q);
; #pragma unroll
;                         for (int r = 0; r < 4; ++r) rank += (t4[r] > key) ? 1 : 0; }
;                     if (rank < 4) TOP[tq * 4 + rank] = s;
;                     asm volatile("s_waitcnt lgkmcnt(0)" ::: "memory");
;                     if (rank < 4) {
;                         const f32x4 tv = *(const LAS f32x4*)(TOP + tq * 4);
;                         const float es = 1.0f + __expf(tv[1] - tv[0]) + __expf(tv[2] - tv[0]) + __expf(tv[3] - tv[0]);
;                         const float wgt = __expf(s - tv[0]) * (1.0f / es);
;                         const int lp = atomicAdd((int*)(LCNT + e), 1);
;                         REC[(nbatch * 16 + tq) * 4 + rank] = (i32x4){e, lp, __float_as_int(wgt), bi * 16 + tq}; }
;                 }
;             }
	ds_read2st64_b32 v[2:3], v108 offset1:8
	ds_read2st64_b32 v[86:87], v108 offset0:16 offset1:24
	ds_read2st64_b32 v[88:89], v108 offset0:32 offset1:40
	ds_read2st64_b32 v[90:91], v108 offset0:48 offset1:56
	s_waitcnt lgkmcnt(3)
	v_add_f32_e32 v1, v249, v2
	v_add_f32_e32 v1, v1, v3
	s_waitcnt lgkmcnt(2)
	v_add_f32_e32 v1, v1, v86
	v_add_f32_e32 v1, v1, v87
	s_waitcnt lgkmcnt(1)
	v_add_f32_e32 v1, v1, v88
	v_add_f32_e32 v1, v1, v89
	s_waitcnt lgkmcnt(0)
	v_add_f32_e32 v1, v1, v90
	v_add_f32_e32 v1, v1, v91
	v_not_b32_e32 v2, v1
	v_or_b32_e32 v3, 0x80000000, v1
	v_cmp_gt_i32_e32 vcc, 0, v1
	s_nop 1
	v_cndmask_b32_e32 v2, v3, v2, vcc
	v_and_b32_e32 v2, 0xffffffe0, v2
	v_bitop3_b32 v2, v2, 31, v0 bitop3:0x36
	ds_write_b32 v109, v2
	s_waitcnt lgkmcnt(0)
	ds_read_b128 v[86:89], v111
	ds_read_b128 v[90:93], v111 offset:16
	ds_read_b128 v[116:119], v111 offset:32
	ds_read_b128 v[120:123], v111 offset:48
	s_waitcnt lgkmcnt(3)
	v_cmp_gt_u32_e32 vcc, v87, v2
	s_nop 1
	v_cndmask_b32_e64 v3, 0, 1, vcc
	v_cmp_gt_u32_e32 vcc, v88, v2
	s_nop 1
	v_cndmask_b32_e64 v87, 0, 1, vcc
	s_waitcnt lgkmcnt(2)
	v_cmp_gt_u32_e32 vcc, v90, v2
	s_nop 1
	v_cndmask_b32_e64 v88, 0, 1, vcc
	v_cmp_gt_u32_e32 vcc, v86, v2
	s_nop 1
	v_addc_co_u32_e32 v3, vcc, 0, v3, vcc
	v_cmp_gt_u32_e32 vcc, v89, v2
	s_nop 1
	v_addc_co_u32_e32 v3, vcc, v3, v87, vcc
	v_cmp_gt_u32_e32 vcc, v91, v2
	s_nop 1
	v_addc_co_u32_e32 v3, vcc, v3, v88, vcc
	v_cmp_gt_u32_e32 vcc, v92, v2
	s_nop 1
	v_cndmask_b32_e64 v86, 0, 1, vcc
	v_cmp_gt_u32_e32 vcc, v93, v2
	s_nop 1
	v_addc_co_u32_e32 v3, vcc, v3, v86, vcc
	s_waitcnt lgkmcnt(1)
	v_cmp_gt_u32_e32 vcc, v116, v2
	s_nop 1
	v_cndmask_b32_e64 v86, 0, 1, vcc
	v_cmp_gt_u32_e32 vcc, v117, v2
	s_nop 1
	v_addc_co_u32_e32 v3, vcc, v3, v86, vcc
	v_cmp_gt_u32_e32 vcc, v118, v2
	s_nop 1
	v_cndmask_b32_e64 v86, 0, 1, vcc
	v_cmp_gt_u32_e32 vcc, v119, v2
	s_nop 1
	v_addc_co_u32_e32 v3, vcc, v3, v86, vcc
	s_waitcnt lgkmcnt(0)
	v_cmp_gt_u32_e32 vcc, v120, v2
	s_nop 1
	v_cndmask_b32_e64 v86, 0, 1, vcc
	v_cmp_gt_u32_e32 vcc, v121, v2
	s_nop 1
	v_addc_co_u32_e32 v3, vcc, v3, v86, vcc
	ds_read_b128 v[86:89], v111 offset:64
	v_cmp_gt_u32_e32 vcc, v122, v2
	s_nop 1
	v_cndmask_b32_e64 v90, 0, 1, vcc
	v_cmp_gt_u32_e32 vcc, v123, v2
	s_nop 1
	v_addc_co_u32_e32 v3, vcc, v3, v90, vcc
	ds_read_b128 v[90:93], v111 offset:80
	s_waitcnt lgkmcnt(1)
	v_cmp_gt_u32_e32 vcc, v86, v2
	s_nop 1
	v_cndmask_b32_e64 v86, 0, 1, vcc
	v_cmp_gt_u32_e32 vcc, v87, v2
	s_nop 1
	v_addc_co_u32_e32 v3, vcc, v3, v86, vcc
	v_cmp_gt_u32_e32 vcc, v88, v2
	s_nop 1
	v_cndmask_b32_e64 v86, 0, 1, vcc
	v_cmp_gt_u32_e32 vcc, v89, v2
	s_nop 1
	v_addc_co_u32_e32 v3, vcc, v3, v86, vcc
	s_waitcnt lgkmcnt(0)
	v_cmp_gt_u32_e32 vcc, v90, v2
	s_nop 1
	v_cndmask_b32_e64 v86, 0, 1, vcc
	v_cmp_gt_u32_e32 vcc, v91, v2
	s_nop 1
	v_addc_co_u32_e32 v3, vcc, v3, v86, vcc
	ds_read_b128 v[86:89], v111 offset:96
	v_cmp_gt_u32_e32 vcc, v92, v2
	s_nop 1
	v_cndmask_b32_e64 v90, 0, 1, vcc
	v_cmp_gt_u32_e32 vcc, v93, v2
	s_nop 1
	v_addc_co_u32_e32 v3, vcc, v3, v90, vcc
	ds_read_b128 v[90:93], v111 offset:112
	s_waitcnt lgkmcnt(1)
	v_cmp_gt_u32_e32 vcc, v86, v2
	s_nop 1
	v_cndmask_b32_e64 v86, 0, 1, vcc
	v_cmp_gt_u32_e32 vcc, v87, v2
	s_nop 1
	v_addc_co_u32_e32 v3, vcc, v3, v86, vcc
	v_cmp_gt_u32_e32 vcc, v88, v2
	s_nop 1
	v_cndmask_b32_e64 v86, 0, 1, vcc
	v_cmp_gt_u32_e32 vcc, v89, v2
	s_nop 1
	v_addc_co_u32_e32 v3, vcc, v3, v86, vcc
	s_waitcnt lgkmcnt(0)
	v_cmp_gt_u32_e32 vcc, v90, v2
	s_nop 1
	v_cndmask_b32_e64 v86, 0, 1, vcc
	v_cmp_gt_u32_e32 vcc, v91, v2
	s_nop 1
	v_addc_co_u32_e32 v3, vcc, v3, v86, vcc
	v_cmp_gt_u32_e32 vcc, v92, v2
	s_nop 1
	v_cndmask_b32_e64 v86, 0, 1, vcc
	v_cmp_gt_u32_e32 vcc, v93, v2
	s_nop 1
	v_addc_co_u32_e32 v86, vcc, v3, v86, vcc
	v_cmp_gt_u32_e32 vcc, 4, v86
	s_and_saveexec_b64 s[6:7], vcc
	v_lshl_add_u32 v2, v86, 2, v112
	ds_write_b32 v2, v1
	s_or_b64 exec, exec, s[6:7]
	s_waitcnt lgkmcnt(0)
	s_and_saveexec_b64 s[6:7], vcc
	s_cbranch_execz .LBB0_493
	ds_read_b128 v[88:91], v112
	v_lshl_add_u32 v86, v86, 4, v32
	s_waitcnt lgkmcnt(0)
	v_sub_f32_e32 v2, v89, v88
	v_sub_f32_e32 v3, v90, v88
	v_mul_f32_e32 v2, 0x3fb8aa3b, v2
	v_sub_f32_e32 v87, v91, v88
	v_mul_f32_e32 v3, 0x3fb8aa3b, v3
	v_exp_f32_e32 v2, v2
	v_mul_f32_e32 v87, 0x3fb8aa3b, v87
	v_exp_f32_e32 v3, v3
	v_exp_f32_e32 v87, v87
	v_add_f32_e32 v2, 1.0, v2
	v_sub_f32_e32 v1, v1, v88
	v_add_f32_e32 v2, v3, v2
	v_add_f32_e32 v2, v87, v2
	v_div_scale_f32 v3, s[10:11], v2, v2, 1.0
	v_rcp_f32_e32 v87, v3
	v_mul_f32_e32 v1, 0x3fb8aa3b, v1
	v_exp_f32_e32 v88, v1
	v_readlane_b32 s10, v255, 36
	v_fma_f32 v1, -v3, v87, 1.0
	v_fmac_f32_e32 v87, v1, v87
	v_div_scale_f32 v1, vcc, 1.0, v2, 1.0
	v_mul_f32_e32 v89, v1, v87
	v_fma_f32 v90, -v3, v89, v1
	v_fmac_f32_e32 v89, v90, v87
	v_fma_f32 v1, -v3, v89, v1
	v_div_fmas_f32 v3, v1, v87, v89
	ds_add_rtn_u32 v1, v110, v203
	v_div_fixup_f32 v2, v3, v2, 1.0
	v_mul_f32_e32 v2, v88, v2
	v_add_u32_e32 v3, s10, v95
	s_waitcnt lgkmcnt(0)
	ds_write_b128 v86, v[0:3]
.LBB0_493:
	s_or_b64 exec, exec, s[6:7]
	v_readlane_b32 s6, v253, 56
	s_add_i32 s12, s12, 1
	s_add_i32 s14, s14, s6
	v_add_u32_e32 v95, s6, v95
	v_add_u32_e32 v32, 0x400, v32
	s_add_i32 s13, s13, 64
	s_and_b64 vcc, exec, s[8:9]
	s_cbranch_vccnz .LBB0_495
	s_branch .LBB0_485
